# v75 + fox softmax stage (lever: VALU instruction selection): probabilities in adjacent register pairs, row sum by 15 v_pk_add_f32 + 2 adds instead of 27 mixed adds
# baseline (speedup 1.0000x reference)
.LBB0_304:
	v_exp_f32_e32 v140, v48
	v_exp_f32_e32 v141, v32
	v_exp_f32_e32 v142, v49
	v_exp_f32_e32 v143, v33
	v_exp_f32_e32 v144, v50
	v_exp_f32_e32 v145, v34
	v_pk_add_f32 v[246:247], v[140:141], v[142:143]
	v_exp_f32_e32 v146, v51
	v_exp_f32_e32 v147, v35
	v_pk_add_f32 v[246:247], v[246:247], v[144:145]
	v_exp_f32_e32 v148, v52
	v_exp_f32_e32 v149, v36
	v_pk_add_f32 v[246:247], v[246:247], v[146:147]
	v_exp_f32_e32 v150, v53
	v_exp_f32_e32 v151, v37
	v_pk_add_f32 v[246:247], v[246:247], v[148:149]
	v_exp_f32_e32 v152, v54
	v_exp_f32_e32 v153, v38
	v_pk_add_f32 v[246:247], v[246:247], v[150:151]
	v_exp_f32_e32 v154, v55
	v_exp_f32_e32 v155, v39
	v_pk_add_f32 v[246:247], v[246:247], v[152:153]
	v_exp_f32_e32 v156, v56
	v_exp_f32_e32 v157, v40
	v_pk_add_f32 v[246:247], v[246:247], v[154:155]
	v_exp_f32_e32 v158, v57
	v_exp_f32_e32 v159, v41
	v_pk_add_f32 v[246:247], v[246:247], v[156:157]
	v_exp_f32_e32 v160, v58
	v_exp_f32_e32 v161, v42
	v_pk_add_f32 v[246:247], v[246:247], v[158:159]
	v_exp_f32_e32 v162, v59
	v_exp_f32_e32 v163, v43
	v_pk_add_f32 v[246:247], v[246:247], v[160:161]
	v_exp_f32_e32 v164, v60
	v_exp_f32_e32 v165, v44
	v_pk_add_f32 v[246:247], v[246:247], v[162:163]
	v_exp_f32_e32 v166, v61
	v_exp_f32_e32 v167, v45
	v_pk_add_f32 v[246:247], v[246:247], v[164:165]
	v_exp_f32_e32 v168, v62
	v_exp_f32_e32 v169, v46
	v_pk_add_f32 v[246:247], v[246:247], v[166:167]
	v_exp_f32_e32 v170, v63
	v_exp_f32_e32 v171, v47
	v_pk_add_f32 v[246:247], v[246:247], v[168:169]
	v_add_u32_e32 v239, v239, v187
	v_cvt_pk_bf16_f32 v32, v140, v142
	v_cvt_pk_bf16_f32 v33, v144, v146
	ds_read_b64_tr_b16 v[48:49],v241 offset:4096
	v_cvt_pk_bf16_f32 v34, v148, v150
	v_cvt_pk_bf16_f32 v35, v152, v154
	ds_read_b64_tr_b16 v[50:51],v241 offset:4608
	v_pk_add_f32 v[246:247], v[246:247], v[170:171]
	v_cvt_pk_bf16_f32 v36, v156, v158
	v_cvt_pk_bf16_f32 v37, v160, v162
	ds_read_b64_tr_b16 v[52:53],v241 offset:5120
	v_cvt_pk_bf16_f32 v38, v164, v166
	v_cvt_pk_bf16_f32 v40, v141, v143
	ds_read_b64_tr_b16 v[54:55],v241 offset:5632
	v_cvt_pk_bf16_f32 v41, v145, v147
	v_cvt_pk_bf16_f32 v42, v149, v151
	ds_read_b64_tr_b16 v[56:57],v241 offset:6144
	v_cvt_pk_bf16_f32 v43, v153, v155
	v_cvt_pk_bf16_f32 v44, v157, v159
	ds_read_b64_tr_b16 v[58:59],v241 offset:6656
	v_cvt_pk_bf16_f32 v45, v161, v163
	v_cvt_pk_bf16_f32 v46, v165, v167
	ds_read_b64_tr_b16 v[60:61],v241 offset:7168
	v_cvt_pk_bf16_f32 v39, v168, v170
	v_cvt_pk_bf16_f32 v47, v169, v171
	ds_read_b64_tr_b16 v[62:63],v241 offset:7680
	s_waitcnt lgkmcnt(8)
	v_add_f32_e32 v248, v246, v247
	v_add_f32_e32 v125, v125, v248
	v_mfma_f32_32x32x16_bf16 v[0:15], v[32:35], v[92:95], v[0:15]
	s_waitcnt lgkmcnt(0)
	v_mfma_f32_32x32x16_bf16 v[0:15], v[36:39], v[88:91], v[0:15]
	v_mfma_f32_32x32x16_bf16 v[0:15], v[40:43], v[84:87], v[0:15]
	v_mfma_f32_32x32x16_bf16 v[0:15], v[44:47], v[80:83], v[0:15]
	v_mfma_f32_32x32x16_bf16 v[16:31], v[32:35], v[48:51], v[16:31]
	s_add_i32 s8, s79, 1
	s_add_i32 s78, s78, 1
	s_and_b32 s79, s8, 3
	s_add_i32 s8, s51, s78
	s_cmp_ge_i32 s8, s75
	v_add_u32_e32 v240, 64, v240
	v_mfma_f32_32x32x16_bf16 v[16:31], v[36:39], v[52:55], v[16:31]
	v_mfma_f32_32x32x16_bf16 v[16:31], v[40:43], v[56:59], v[16:31]
	v_mfma_f32_32x32x16_bf16 v[16:31], v[44:47], v[60:63], v[16:31]
	s_cbranch_scc1 .LBB0_312
	s_nop 0
	v_mov_b32_e32 v242, v243
	s_andn2_b64 vcc, exec, s[28:29]
	s_add_i32 s42, s51, s78
	s_cbranch_vccz .LBB0_283
	s_branch .LBB0_287
